# back-edge rotation of the GQA and differential-attention tile loops: loop-back barrier becomes the loop head, exit test and head scalar arithmetic moved in front of it, exit path gets its own barrier
# speedup vs baseline: 1.0011x; 1.0011x over previous
.LBB0_317:
	v_lshrrev_b32_e32 v92, 2, v234
	v_bitop3_b32 v90, v90, v92, 3 bitop3:0x78
	v_lshlrev_b32_e32 v91, 6, v233
	s_add_i32 s6, 0, 0x8000
	v_lshlrev_b32_e32 v90, 4, v90
	v_add3_u32 v241, v91, s6, v90
	v_and_b32_e32 v235, 15, v234
	v_bfe_u32 v90, v234, 4, 1
	v_cmp_eq_u32_e32 vcc, v90, v235
	v_mov_b32_e32 v122, v211
	v_mov_b32_e32 v123, v211
	s_waitcnt vmcnt(0)
	v_cndmask_b32_e32 v114, 0, v85, vcc
	v_lshlrev_b32_e32 v85, 16, v78
	v_and_b32_e32 v78, 0xffff0000, v78
	v_mul_f32_e32 v85, 0x3eb6d5d0, v85
	v_mul_f32_e32 v78, 0x3eb6d5d0, v78
	v_cvt_pk_fp8_f32 v122, v85, v78
	v_lshlrev_b32_e32 v78, 16, v79
	v_and_b32_e32 v79, 0xffff0000, v79
	v_mul_f32_e32 v78, 0x3eb6d5d0, v78
	v_mul_f32_e32 v79, 0x3eb6d5d0, v79
	v_cvt_pk_fp8_f32 v122, v78, v79 op_sel:[0,0,1]
	v_lshlrev_b32_e32 v78, 16, v80
	v_and_b32_e32 v79, 0xffff0000, v80
	v_mul_f32_e32 v78, 0x3eb6d5d0, v78
	v_mul_f32_e32 v79, 0x3eb6d5d0, v79
	v_cvt_pk_fp8_f32 v123, v78, v79
	v_lshlrev_b32_e32 v78, 16, v81
	v_and_b32_e32 v79, 0xffff0000, v81
	v_mul_f32_e32 v78, 0x3eb6d5d0, v78
	v_mul_f32_e32 v79, 0x3eb6d5d0, v79
	v_cvt_pk_fp8_f32 v123, v78, v79 op_sel:[0,0,1]
	v_lshlrev_b32_e32 v78, 16, v74
	v_and_b32_e32 v74, 0xffff0000, v74
	v_mul_f32_e32 v78, 0x3eb6d5d0, v78
	v_mul_f32_e32 v74, 0x3eb6d5d0, v74
	v_mov_b32_e32 v124, v211
	v_cvt_pk_fp8_f32 v124, v78, v74
	v_lshlrev_b32_e32 v74, 16, v75
	v_and_b32_e32 v75, 0xffff0000, v75
	v_mul_f32_e32 v74, 0x3eb6d5d0, v74
	v_mul_f32_e32 v75, 0x3eb6d5d0, v75
	v_cvt_pk_fp8_f32 v124, v74, v75 op_sel:[0,0,1]
	v_lshlrev_b32_e32 v74, 16, v76
	v_and_b32_e32 v75, 0xffff0000, v76
	v_mul_f32_e32 v74, 0x3eb6d5d0, v74
	v_mul_f32_e32 v75, 0x3eb6d5d0, v75
	v_mov_b32_e32 v125, v211
	v_cvt_pk_fp8_f32 v125, v74, v75
	v_lshlrev_b32_e32 v74, 16, v77
	v_and_b32_e32 v75, 0xffff0000, v77
	v_mul_f32_e32 v74, 0x3eb6d5d0, v74
	v_mul_f32_e32 v75, 0x3eb6d5d0, v75
	v_cvt_pk_fp8_f32 v125, v74, v75 op_sel:[0,0,1]
	v_lshlrev_b32_e32 v74, 16, v70
	v_and_b32_e32 v70, 0xffff0000, v70
	v_mul_f32_e32 v74, 0x3eb6d5d0, v74
	v_mul_f32_e32 v70, 0x3eb6d5d0, v70
	v_mov_b32_e32 v126, v211
	v_cvt_pk_fp8_f32 v126, v74, v70
	v_lshlrev_b32_e32 v70, 16, v71
	v_and_b32_e32 v71, 0xffff0000, v71
	v_mul_f32_e32 v70, 0x3eb6d5d0, v70
	v_mul_f32_e32 v71, 0x3eb6d5d0, v71
	v_cvt_pk_fp8_f32 v126, v70, v71 op_sel:[0,0,1]
	v_lshlrev_b32_e32 v70, 16, v72
	v_and_b32_e32 v71, 0xffff0000, v72
	v_mul_f32_e32 v70, 0x3eb6d5d0, v70
	v_mul_f32_e32 v71, 0x3eb6d5d0, v71
	v_mov_b32_e32 v127, v211
	v_cvt_pk_fp8_f32 v127, v70, v71
	v_lshlrev_b32_e32 v70, 16, v73
	v_and_b32_e32 v71, 0xffff0000, v73
	v_mul_f32_e32 v70, 0x3eb6d5d0, v70
	v_mul_f32_e32 v71, 0x3eb6d5d0, v71
	v_cvt_pk_fp8_f32 v127, v70, v71 op_sel:[0,0,1]
	v_lshlrev_b32_e32 v70, 16, v66
	v_and_b32_e32 v66, 0xffff0000, v66
	v_mul_f32_e32 v70, 0x3eb6d5d0, v70
	v_mul_f32_e32 v66, 0x3eb6d5d0, v66
	v_mov_b32_e32 v128, v211
	v_cvt_pk_fp8_f32 v128, v70, v66
	v_lshlrev_b32_e32 v66, 16, v67
	v_and_b32_e32 v67, 0xffff0000, v67
	v_mul_f32_e32 v66, 0x3eb6d5d0, v66
	v_mul_f32_e32 v67, 0x3eb6d5d0, v67
	v_cvt_pk_fp8_f32 v128, v66, v67 op_sel:[0,0,1]
	v_lshlrev_b32_e32 v66, 16, v68
	v_and_b32_e32 v67, 0xffff0000, v68
	v_mul_f32_e32 v66, 0x3eb6d5d0, v66
	v_mul_f32_e32 v67, 0x3eb6d5d0, v67
	v_mov_b32_e32 v129, v211
	v_cvt_pk_fp8_f32 v129, v66, v67
	v_lshlrev_b32_e32 v66, 16, v69
	v_and_b32_e32 v67, 0xffff0000, v69
	v_mul_f32_e32 v66, 0x3eb6d5d0, v66
	v_mul_f32_e32 v67, 0x3eb6d5d0, v67
	v_cvt_pk_fp8_f32 v129, v66, v67 op_sel:[0,0,1]
	v_lshlrev_b32_e32 v66, 16, v46
	v_and_b32_e32 v46, 0xffff0000, v46
	v_mul_f32_e32 v66, 0x3eb6d5d0, v66
	v_mul_f32_e32 v46, 0x3eb6d5d0, v46
	v_mov_b32_e32 v130, v211
	v_cvt_pk_fp8_f32 v130, v66, v46
	v_lshlrev_b32_e32 v46, 16, v47
	v_and_b32_e32 v47, 0xffff0000, v47
	v_mul_f32_e32 v46, 0x3eb6d5d0, v46
	v_mul_f32_e32 v47, 0x3eb6d5d0, v47
	v_cvt_pk_fp8_f32 v130, v46, v47 op_sel:[0,0,1]
	v_lshlrev_b32_e32 v46, 16, v48
	v_and_b32_e32 v47, 0xffff0000, v48
	v_mul_f32_e32 v46, 0x3eb6d5d0, v46
	v_mul_f32_e32 v47, 0x3eb6d5d0, v47
	v_mov_b32_e32 v131, v211
	v_cvt_pk_fp8_f32 v131, v46, v47
	v_lshlrev_b32_e32 v46, 16, v49
	v_and_b32_e32 v47, 0xffff0000, v49
	v_mul_f32_e32 v46, 0x3eb6d5d0, v46
	v_mul_f32_e32 v47, 0x3eb6d5d0, v47
	v_cvt_pk_fp8_f32 v131, v46, v47 op_sel:[0,0,1]
	v_lshlrev_b32_e32 v46, 16, v42
	v_and_b32_e32 v42, 0xffff0000, v42
	v_mul_f32_e32 v46, 0x3eb6d5d0, v46
	v_mul_f32_e32 v42, 0x3eb6d5d0, v42
	v_mov_b32_e32 v132, v211
	v_cvt_pk_fp8_f32 v132, v46, v42
	v_lshlrev_b32_e32 v42, 16, v43
	v_and_b32_e32 v43, 0xffff0000, v43
	v_mul_f32_e32 v42, 0x3eb6d5d0, v42
	v_mul_f32_e32 v43, 0x3eb6d5d0, v43
	v_cvt_pk_fp8_f32 v132, v42, v43 op_sel:[0,0,1]
	v_lshlrev_b32_e32 v42, 16, v44
	v_and_b32_e32 v43, 0xffff0000, v44
	v_mul_f32_e32 v42, 0x3eb6d5d0, v42
	v_mul_f32_e32 v43, 0x3eb6d5d0, v43
	v_mov_b32_e32 v133, v211
	v_cvt_pk_fp8_f32 v133, v42, v43
	v_lshlrev_b32_e32 v42, 16, v45
	v_and_b32_e32 v43, 0xffff0000, v45
	v_mul_f32_e32 v42, 0x3eb6d5d0, v42
	v_mul_f32_e32 v43, 0x3eb6d5d0, v43
	v_cvt_pk_fp8_f32 v133, v42, v43 op_sel:[0,0,1]
	v_lshlrev_b32_e32 v42, 16, v38
	v_and_b32_e32 v38, 0xffff0000, v38
	v_mul_f32_e32 v42, 0x3eb6d5d0, v42
	v_mul_f32_e32 v38, 0x3eb6d5d0, v38
	v_mov_b32_e32 v134, v211
	v_cvt_pk_fp8_f32 v134, v42, v38
	v_lshlrev_b32_e32 v38, 16, v39
	v_and_b32_e32 v39, 0xffff0000, v39
	v_mul_f32_e32 v38, 0x3eb6d5d0, v38
	v_mul_f32_e32 v39, 0x3eb6d5d0, v39
	v_cvt_pk_fp8_f32 v134, v38, v39 op_sel:[0,0,1]
	v_lshlrev_b32_e32 v38, 16, v40
	v_and_b32_e32 v39, 0xffff0000, v40
	v_mul_f32_e32 v38, 0x3eb6d5d0, v38
	v_mul_f32_e32 v39, 0x3eb6d5d0, v39
	v_mov_b32_e32 v135, v211
	v_cvt_pk_fp8_f32 v135, v38, v39
	v_lshlrev_b32_e32 v38, 16, v41
	v_and_b32_e32 v39, 0xffff0000, v41
	v_mul_f32_e32 v38, 0x3eb6d5d0, v38
	v_mul_f32_e32 v39, 0x3eb6d5d0, v39
	v_cvt_pk_fp8_f32 v135, v38, v39 op_sel:[0,0,1]
	v_lshlrev_b32_e32 v38, 16, v34
	v_and_b32_e32 v34, 0xffff0000, v34
	v_mul_f32_e32 v38, 0x3eb6d5d0, v38
	v_mul_f32_e32 v34, 0x3eb6d5d0, v34
	v_mov_b32_e32 v136, v211
	v_cvt_pk_fp8_f32 v136, v38, v34
	v_lshlrev_b32_e32 v34, 16, v35
	v_and_b32_e32 v35, 0xffff0000, v35
	v_mul_f32_e32 v34, 0x3eb6d5d0, v34
	v_mul_f32_e32 v35, 0x3eb6d5d0, v35
	v_cvt_pk_fp8_f32 v136, v34, v35 op_sel:[0,0,1]
	v_lshlrev_b32_e32 v34, 16, v36
	v_and_b32_e32 v35, 0xffff0000, v36
	v_mul_f32_e32 v34, 0x3eb6d5d0, v34
	v_mul_f32_e32 v35, 0x3eb6d5d0, v35
	v_mov_b32_e32 v137, v211
	v_cvt_pk_fp8_f32 v137, v34, v35
	v_lshlrev_b32_e32 v34, 16, v37
	v_and_b32_e32 v35, 0xffff0000, v37
	v_mul_f32_e32 v34, 0x3eb6d5d0, v34
	v_mul_f32_e32 v35, 0x3eb6d5d0, v35
	v_cvt_pk_fp8_f32 v137, v34, v35 op_sel:[0,0,1]
	s_ashr_i32 s41, s40, 31
	s_lshl_b32 s2, s2, 7
	s_mov_b32 s4, 0x8000
	v_xor_b32_e32 v240, 16, v241
	v_cndmask_b32_e32 v115, 0, v86, vcc
	v_cndmask_b32_e32 v116, 0, v87, vcc
	v_cndmask_b32_e32 v117, 0, v88, vcc
	v_cndmask_b32_e32 v118, 0, v89, vcc
	v_cndmask_b32_e32 v119, 0, v82, vcc
	v_cndmask_b32_e32 v120, 0, v83, vcc
	v_cndmask_b32_e32 v121, 0, v84, vcc
	s_waitcnt lgkmcnt(0)
	v_mfma_scale_f32_32x32x64_f8f6f4 v[34:49], v[26:33], v[122:129], v[2:17], v213, v213 op_sel_hi:[0,0,0]
	v_mfma_scale_f32_32x32x64_f8f6f4 v[18:33], v[18:25], v[122:129], v[2:17], v213, v213 op_sel_hi:[0,0,0]
	v_mfma_scale_f32_32x32x64_f8f6f4 v[34:49], v[58:65], v[130:137], v[34:49], v213, v213 op_sel_hi:[0,0,0]
	v_mfma_scale_f32_32x32x64_f8f6f4 v[18:33], v[50:57], v[130:137], v[18:33], v213, v213 op_sel_hi:[0,0,0]
	s_barrier
	v_add_u32_e32 v50, 0x2000, v236
	ds_read_b128 v[178:181], v50 offset:0
	v_add_u32_e32 v51, 0x2000, v237
	ds_read_b128 v[182:185], v51 offset:0
	ds_read_b128 v[194:197], v50 offset:0x1000
	ds_read_b128 v[198:201], v51 offset:0x1000
	v_add_u32_e32 v50, 0x2000, v238
	ds_read_b128 v[186:189], v50 offset:0
	v_add_u32_e32 v51, 0x2000, v239
	ds_read_b128 v[190:193], v51 offset:0
	ds_read_b128 v[170:173], v50 offset:0x1000
	ds_read_b128 v[174:177], v51 offset:0x1000
	ds_read_b128 v[154:157], v241 offset:0
	ds_read_b128 v[158:161], v240 offset:0
	ds_read_b128 v[146:149], v241 offset:0x800
	ds_read_b128 v[150:153], v240 offset:0x800
	ds_read_b128 v[138:141], v241 offset:0x1000
	ds_read_b128 v[142:145], v240 offset:0x1000
	s_mov_b64 s[6:7], 0xc000
	v_lshl_add_u64 v[50:51], v[218:219], 0, s[6:7]
	s_add_i32 m0, s3, 0x6000
	s_mov_b64 s[6:7], 0xe000
	global_load_lds_dwordx4 v[50:51], off
	v_lshl_add_u64 v[50:51], v[218:219], 0, s[6:7]
	s_add_i32 m0, s3, 0xe000
	s_nop 7
	v_cvt_pk_u8_f32 v18, v18, 0, 0
	global_load_lds_dwordx4 v[50:51], off
	v_cvt_pk_u8_f32 v34, v34, 0, 0
	v_cvt_pk_u8_f32 v18, v19, 1, v18
	v_cvt_pk_u8_f32 v34, v35, 1, v34
	v_cvt_pk_u8_f32 v18, v20, 2, v18
	v_cvt_pk_u8_f32 v34, v36, 2, v34
	v_cvt_pk_u8_f32 v166, v21, 3, v18
	v_cvt_pk_u8_f32 v18, v22, 0, 0
	v_cvt_pk_u8_f32 v162, v37, 3, v34
	v_cvt_pk_u8_f32 v34, v38, 0, 0
	v_cvt_pk_u8_f32 v18, v23, 1, v18
	v_cvt_pk_u8_f32 v34, v39, 1, v34
	v_cvt_pk_u8_f32 v18, v24, 2, v18
	v_cvt_pk_u8_f32 v34, v40, 2, v34
	v_cvt_pk_u8_f32 v167, v25, 3, v18
	v_cvt_pk_u8_f32 v18, v26, 0, 0
	v_cvt_pk_u8_f32 v163, v41, 3, v34
	v_cvt_pk_u8_f32 v34, v42, 0, 0
	v_cvt_pk_u8_f32 v18, v27, 1, v18
	v_cvt_pk_u8_f32 v34, v43, 1, v34
	v_cvt_pk_u8_f32 v18, v28, 2, v18
	v_cvt_pk_u8_f32 v34, v44, 2, v34
	v_cvt_pk_u8_f32 v168, v29, 3, v18
	v_cvt_pk_u8_f32 v18, v30, 0, 0
	v_cvt_pk_u8_f32 v164, v45, 3, v34
	v_cvt_pk_u8_f32 v34, v46, 0, 0
	v_cvt_pk_u8_f32 v18, v31, 1, v18
	s_waitcnt vmcnt(2)
	v_cvt_pk_u8_f32 v34, v47, 1, v34
	v_cvt_pk_u8_f32 v18, v32, 2, v18
	v_cvt_pk_u8_f32 v34, v48, 2, v34
	v_cvt_pk_u8_f32 v169, v33, 3, v18
	v_mov_b32_e32 v18, 0
	s_add_i32 s5, s5, -1
	v_cvt_pk_u8_f32 v165, v49, 3, v34
	s_mov_b32 s6, 0
	v_mov_b32_e32 v19, v18
	v_mov_b32_e32 v20, v18
	v_mov_b32_e32 v21, v18
	v_mov_b32_e32 v22, v18
	v_mov_b32_e32 v23, v18
	v_mov_b32_e32 v24, v18
	v_mov_b32_e32 v25, v18
	v_mov_b32_e32 v26, v18
	v_mov_b32_e32 v27, v18
	v_mov_b32_e32 v28, v18
	v_mov_b32_e32 v29, v18
	v_mov_b32_e32 v30, v18
	v_mov_b32_e32 v31, v18
	v_mov_b32_e32 v32, v18
	v_mov_b32_e32 v33, v18
	v_mov_b32_e32 v34, v18
	v_mov_b32_e32 v35, v18
	v_mov_b32_e32 v36, v18
	v_mov_b32_e32 v37, v18
	v_mov_b32_e32 v38, v18
	v_mov_b32_e32 v39, v18
	v_mov_b32_e32 v40, v18
	v_mov_b32_e32 v41, v18
	v_mov_b32_e32 v42, v18
	v_mov_b32_e32 v43, v18
	v_mov_b32_e32 v44, v18
	v_mov_b32_e32 v45, v18
	v_mov_b32_e32 v46, v18
	v_mov_b32_e32 v47, v18
	v_mov_b32_e32 v48, v18
	v_mov_b32_e32 v49, v18
	v_mov_b32_e32 v50, v18
	v_mov_b32_e32 v51, v18
	v_mov_b32_e32 v52, v18
	v_mov_b32_e32 v53, v18
	v_mov_b32_e32 v54, v18
	v_mov_b32_e32 v55, v18
	v_mov_b32_e32 v56, v18
	v_mov_b32_e32 v57, v18
	v_mov_b32_e32 v58, v18
	v_mov_b32_e32 v59, v18
	v_mov_b32_e32 v60, v18
	v_mov_b32_e32 v61, v18
	v_mov_b32_e32 v62, v18
	v_mov_b32_e32 v63, v18
	v_mov_b32_e32 v64, v18
	v_mov_b32_e32 v65, v18
	v_mov_b32_e32 v202, v18
	v_mov_b32_e32 v203, v18
	v_mov_b32_e32 v204, v18
	v_mov_b32_e32 v205, v18
	v_mov_b32_e32 v66, v18
	v_mov_b32_e32 v67, v18
	v_mov_b32_e32 v68, v18
	v_mov_b32_e32 v69, v18
	v_mov_b32_e32 v70, v18
	v_mov_b32_e32 v71, v18
	v_mov_b32_e32 v72, v18
	v_mov_b32_e32 v73, v18
	v_mov_b32_e32 v74, v18
	v_mov_b32_e32 v75, v18
	v_mov_b32_e32 v76, v18
	v_mov_b32_e32 v77, v18
	v_mov_b32_e32 v78, v18
	v_mov_b32_e32 v79, v18
	v_mov_b32_e32 v80, v18
	v_mov_b32_e32 v81, v18
	s_add_i32 s7, s4, 0xffffa000
	s_add_i32 s26, s4, 0x8000
.Lrot_gqa:
	s_barrier
	s_waitcnt lgkmcnt(0)
	v_mfma_scale_f32_32x32x64_f8f6f4 v[82:97], v[178:185], v[122:129], v[2:17], v213, v213 op_sel_hi:[0,0,0]
	s_and_b32 s26, s26, 0xe000
	v_mfma_scale_f32_32x32x64_f8f6f4 v[98:113], v[194:201], v[122:129], v[2:17], v213, v213 op_sel_hi:[0,0,0]
	v_mfma_scale_f32_32x32x64_f8f6f4 v[82:97], v[186:193], v[130:137], v[82:97], v213, v213 op_sel_hi:[0,0,0]
	v_mfma_scale_f32_32x32x64_f8f6f4 v[98:113], v[170:177], v[130:137], v[98:113], v213, v213 op_sel_hi:[0,0,0]
	v_mfma_scale_f32_32x32x64_f8f6f4 v[66:81], v[162:169], v[154:161], v[66:81], v221, v220 op_sel_hi:[0,0,0] cbsz:1
	v_add_u32_e32 v158, s26, v241
	ds_read_b128 v[154:157], v158 offset:0x1800
	v_add_u32_e32 v170, s26, v240
	ds_read_b128 v[158:161], v170 offset:0x1800
	v_mfma_scale_f32_32x32x64_f8f6f4 v[50:65], v[162:169], v[146:153], v[50:65], v221, v220 op_sel_hi:[0,0,0] cbsz:1
	v_mfma_scale_f32_32x32x64_f8f6f4 v[34:49], v[162:169], v[138:145], v[34:49], v221, v220 op_sel_hi:[0,0,0] cbsz:1
	v_mfma_scale_f32_16x16x128_f8f6f4 v[202:205], v[162:169], v[114:121], v[202:205], v221, v221 op_sel_hi:[0,0,0] cbsz:1
	s_waitcnt lgkmcnt(0)
	v_mfma_scale_f32_32x32x64_f8f6f4 v[18:33], v[162:169], v[154:161], v[18:33], v221, v220 op_sel_hi:[0,0,0] cbsz:1
	s_add_i32 s26, s4, 0xffffc000
	s_and_b32 s26, s26, 0x6000
	s_barrier
	v_add_u32_e32 v138, s26, v236
	ds_read_b128 v[178:181], v138 offset:0
	v_add_u32_e32 v139, s26, v237
	ds_read_b128 v[182:185], v139 offset:0
	ds_read_b128 v[194:197], v138 offset:0x1000
	ds_read_b128 v[198:201], v139 offset:0x1000
	v_add_u32_e32 v138, s26, v238
	ds_read_b128 v[186:189], v138 offset:0
	v_add_u32_e32 v139, s26, v239
	ds_read_b128 v[190:193], v139 offset:0
	ds_read_b128 v[170:173], v138 offset:0x1000
	ds_read_b128 v[174:177], v139 offset:0x1000
	s_and_b32 s7, s7, 0xe000
	v_add_u32_e32 v142, s7, v241
	ds_read_b128 v[154:157], v142 offset:0
	v_add_u32_e32 v162, s7, v240
	ds_read_b128 v[158:161], v162 offset:0
	ds_read_b128 v[146:149], v142 offset:0x800
	ds_read_b128 v[150:153], v162 offset:0x800
	ds_read_b128 v[138:141], v142 offset:0x1000
	ds_read_b128 v[142:145], v162 offset:0x1000
	s_add_i32 s7, s6, 4
	s_min_u32 s7, s7, s5
	s_lshl_b32 s80, s7, 14
	s_and_b32 s7, s4, 0x6000
	s_add_i32 m0, s3, s7
	s_and_b32 s7, s4, 0xe000
	v_lshl_add_u64 v[162:163], v[218:219], 0, s[80:81]
	s_add_i32 s7, s3, s7
	global_load_lds_dwordx4 v[162:163], off
	v_lshl_add_u64 v[162:163], v[162:163], 0, s[48:49]
	s_add_i32 m0, s7, 0x8000
	v_cvt_pk_u8_f32 v82, v82, 0, 0
	global_load_lds_dwordx4 v[162:163], off
	v_cvt_pk_u8_f32 v98, v98, 0, 0
	v_cvt_pk_u8_f32 v82, v83, 1, v82
	v_cvt_pk_u8_f32 v83, v99, 1, v98
	v_cvt_pk_u8_f32 v82, v84, 2, v82
	v_cvt_pk_u8_f32 v83, v100, 2, v83
	v_cvt_pk_u8_f32 v162, v85, 3, v82
	v_cvt_pk_u8_f32 v166, v101, 3, v83
	v_cvt_pk_u8_f32 v82, v86, 0, 0
	v_cvt_pk_u8_f32 v83, v102, 0, 0
	v_cvt_pk_u8_f32 v82, v87, 1, v82
	v_cvt_pk_u8_f32 v83, v103, 1, v83
	v_cvt_pk_u8_f32 v82, v88, 2, v82
	v_cvt_pk_u8_f32 v83, v104, 2, v83
	v_cvt_pk_u8_f32 v163, v89, 3, v82
	v_cvt_pk_u8_f32 v167, v105, 3, v83
	v_cvt_pk_u8_f32 v82, v90, 0, 0
	v_cvt_pk_u8_f32 v83, v106, 0, 0
	v_cvt_pk_u8_f32 v82, v91, 1, v82
	v_cvt_pk_u8_f32 v83, v107, 1, v83
	v_cvt_pk_u8_f32 v82, v92, 2, v82
	v_cvt_pk_u8_f32 v83, v108, 2, v83
	v_cvt_pk_u8_f32 v164, v93, 3, v82
	v_cvt_pk_u8_f32 v168, v109, 3, v83
	v_cvt_pk_u8_f32 v82, v94, 0, 0
	v_cvt_pk_u8_f32 v83, v110, 0, 0
	v_cvt_pk_u8_f32 v82, v95, 1, v82
	v_cvt_pk_u8_f32 v83, v111, 1, v83
	s_waitcnt vmcnt(2)
	v_cvt_pk_u8_f32 v82, v96, 2, v82
	v_cvt_pk_u8_f32 v83, v112, 2, v83
	s_addk_i32 s4, 0x2000
	s_add_i32 s6, s6, 1
	s_add_i32 s7, s4, 0xffffa000
	s_add_i32 s26, s4, 0x8000
	v_cvt_pk_u8_f32 v165, v97, 3, v82
	v_cvt_pk_u8_f32 v169, v113, 3, v83
	s_cmp_eq_u32 s5, s6
	s_cbranch_scc0 .Lrot_gqa
	s_barrier
	s_waitcnt vmcnt(0)
	s_waitcnt lgkmcnt(0)
	v_mfma_scale_f32_32x32x64_f8f6f4 v[66:81], v[162:169], v[154:161], v[66:81], v221, v220 op_sel_hi:[0,0,0] cbsz:1
	v_add_u32_e32 v2, 0x6000, v241
	ds_read_b128 v[6:9], v2 offset:0x1800
	v_add_u32_e32 v2, 0x6000, v240
	ds_read_b128 v[10:13], v2 offset:0x1800
	v_mfma_scale_f32_32x32x64_f8f6f4 v[50:65], v[162:169], v[146:153], v[50:65], v221, v220 op_sel_hi:[0,0,0] cbsz:1
	v_mfma_scale_f32_32x32x64_f8f6f4 v[34:49], v[162:169], v[138:145], v[34:49], v221, v220 op_sel_hi:[0,0,0] cbsz:1
	v_mfma_scale_f32_16x16x128_f8f6f4 v[2:5], v[162:169], v[114:121], v[202:205], v221, v221 op_sel_hi:[0,0,0] cbsz:1
	s_waitcnt lgkmcnt(0)
	v_mfma_scale_f32_32x32x64_f8f6f4 v[18:33], v[162:169], v[6:13], v[18:33], v221, v220 op_sel_hi:[0,0,0] cbsz:1
	s_and_b64 vcc, exec, s[38:39]
	s_cbranch_vccz .LBB0_321
	s_barrier

.LBB0_343:
	v_lshrrev_b32_e32 v44, 2, v188
	v_bitop3_b32 v42, v42, v44, 3 bitop3:0x78
	v_lshlrev_b32_e32 v43, 6, v186
	s_add_i32 s27, 0, 0x8000
	v_lshlrev_b32_e32 v42, 4, v42
	v_add3_u32 v192, v43, s27, v42
	v_and_b32_e32 v189, 15, v188
	v_bfe_u32 v42, v188, 4, 1
	v_cmp_eq_u32_e32 vcc, v42, v189
	v_mov_b32_e32 v122, v211
	v_mov_b32_e32 v123, v211
	v_cndmask_b32_e32 v114, 0, v37, vcc
	s_waitcnt vmcnt(0)
	v_lshlrev_b32_e32 v37, 16, v30
	v_and_b32_e32 v30, 0xffff0000, v30
	v_mul_f32_e32 v37, 0x3ed96d09, v37
	v_mul_f32_e32 v30, 0x3ed96d09, v30
	v_cvt_pk_fp8_f32 v122, v37, v30
	v_lshlrev_b32_e32 v30, 16, v31
	v_and_b32_e32 v31, 0xffff0000, v31
	v_mul_f32_e32 v30, 0x3ed96d09, v30
	v_mul_f32_e32 v31, 0x3ed96d09, v31
	v_cvt_pk_fp8_f32 v122, v30, v31 op_sel:[0,0,1]
	v_lshlrev_b32_e32 v30, 16, v32
	v_and_b32_e32 v31, 0xffff0000, v32
	v_mul_f32_e32 v30, 0x3ed96d09, v30
	v_mul_f32_e32 v31, 0x3ed96d09, v31
	v_cvt_pk_fp8_f32 v123, v30, v31
	v_lshlrev_b32_e32 v30, 16, v33
	v_and_b32_e32 v31, 0xffff0000, v33
	v_mul_f32_e32 v30, 0x3ed96d09, v30
	v_mul_f32_e32 v31, 0x3ed96d09, v31
	v_cvt_pk_fp8_f32 v123, v30, v31 op_sel:[0,0,1]
	v_lshlrev_b32_e32 v30, 16, v26
	v_and_b32_e32 v26, 0xffff0000, v26
	v_mul_f32_e32 v30, 0x3ed96d09, v30
	v_mul_f32_e32 v26, 0x3ed96d09, v26
	v_mov_b32_e32 v124, v211
	v_cvt_pk_fp8_f32 v124, v30, v26
	v_lshlrev_b32_e32 v26, 16, v27
	v_and_b32_e32 v27, 0xffff0000, v27
	v_mul_f32_e32 v26, 0x3ed96d09, v26
	v_mul_f32_e32 v27, 0x3ed96d09, v27
	v_cvt_pk_fp8_f32 v124, v26, v27 op_sel:[0,0,1]
	v_lshlrev_b32_e32 v26, 16, v28
	v_and_b32_e32 v27, 0xffff0000, v28
	v_mul_f32_e32 v26, 0x3ed96d09, v26
	v_mul_f32_e32 v27, 0x3ed96d09, v27
	v_mov_b32_e32 v125, v211
	v_cvt_pk_fp8_f32 v125, v26, v27
	v_lshlrev_b32_e32 v26, 16, v29
	v_and_b32_e32 v27, 0xffff0000, v29
	v_mul_f32_e32 v26, 0x3ed96d09, v26
	v_mul_f32_e32 v27, 0x3ed96d09, v27
	v_cvt_pk_fp8_f32 v125, v26, v27 op_sel:[0,0,1]
	v_lshlrev_b32_e32 v26, 16, v22
	v_and_b32_e32 v22, 0xffff0000, v22
	v_mul_f32_e32 v26, 0x3ed96d09, v26
	v_mul_f32_e32 v22, 0x3ed96d09, v22
	v_mov_b32_e32 v126, v211
	v_cvt_pk_fp8_f32 v126, v26, v22
	v_lshlrev_b32_e32 v22, 16, v23
	v_and_b32_e32 v23, 0xffff0000, v23
	v_mul_f32_e32 v22, 0x3ed96d09, v22
	v_mul_f32_e32 v23, 0x3ed96d09, v23
	v_cvt_pk_fp8_f32 v126, v22, v23 op_sel:[0,0,1]
	v_lshlrev_b32_e32 v22, 16, v24
	v_and_b32_e32 v23, 0xffff0000, v24
	v_mul_f32_e32 v22, 0x3ed96d09, v22
	v_mul_f32_e32 v23, 0x3ed96d09, v23
	v_mov_b32_e32 v127, v211
	v_cvt_pk_fp8_f32 v127, v22, v23
	v_lshlrev_b32_e32 v22, 16, v25
	v_and_b32_e32 v23, 0xffff0000, v25
	v_mul_f32_e32 v22, 0x3ed96d09, v22
	v_mul_f32_e32 v23, 0x3ed96d09, v23
	v_cvt_pk_fp8_f32 v127, v22, v23 op_sel:[0,0,1]
	v_lshlrev_b32_e32 v22, 16, v18
	v_and_b32_e32 v18, 0xffff0000, v18
	v_mul_f32_e32 v22, 0x3ed96d09, v22
	v_mul_f32_e32 v18, 0x3ed96d09, v18
	v_mov_b32_e32 v128, v211
	v_cvt_pk_fp8_f32 v128, v22, v18
	v_lshlrev_b32_e32 v18, 16, v19
	v_and_b32_e32 v19, 0xffff0000, v19
	v_mul_f32_e32 v18, 0x3ed96d09, v18
	v_mul_f32_e32 v19, 0x3ed96d09, v19
	v_cvt_pk_fp8_f32 v128, v18, v19 op_sel:[0,0,1]
	v_lshlrev_b32_e32 v18, 16, v20
	v_and_b32_e32 v19, 0xffff0000, v20
	v_mul_f32_e32 v18, 0x3ed96d09, v18
	v_mul_f32_e32 v19, 0x3ed96d09, v19
	v_mov_b32_e32 v129, v211
	v_cvt_pk_fp8_f32 v129, v18, v19
	v_lshlrev_b32_e32 v18, 16, v21
	v_and_b32_e32 v19, 0xffff0000, v21
	v_mul_f32_e32 v18, 0x3ed96d09, v18
	v_mul_f32_e32 v19, 0x3ed96d09, v19
	v_cvt_pk_fp8_f32 v129, v18, v19 op_sel:[0,0,1]
	v_ashrrev_i32_e32 v183, 31, v182
	s_mov_b32 s5, 0x8000
	v_xor_b32_e32 v191, 16, v192
	v_cndmask_b32_e32 v115, 0, v38, vcc
	v_cndmask_b32_e32 v116, 0, v39, vcc
	v_cndmask_b32_e32 v117, 0, v40, vcc
	v_cndmask_b32_e32 v118, 0, v41, vcc
	v_cndmask_b32_e32 v119, 0, v34, vcc
	v_cndmask_b32_e32 v120, 0, v35, vcc
	v_cndmask_b32_e32 v121, 0, v36, vcc
	s_waitcnt lgkmcnt(0)
	v_mfma_scale_f32_32x32x64_f8f6f4 v[18:33], v[2:9], v[122:129], v[66:81], v213, v213 op_sel_hi:[0,0,0]
	v_mfma_scale_f32_32x32x64_f8f6f4 v[2:17], v[10:17], v[122:129], v[66:81], v213, v213 op_sel_hi:[0,0,0]
	s_barrier
	v_add_u32_e32 v34, 0x2000, v190
	ds_read_b128 v[162:165], v34 offset:0
	v_add_u32_e32 v35, 0x2000, v193
	ds_read_b128 v[166:169], v35 offset:0
	ds_read_b128 v[170:173], v34 offset:0x1000
	ds_read_b128 v[174:177], v35 offset:0x1000
	ds_read_b128 v[146:149], v192 offset:0
	ds_read_b128 v[150:153], v191 offset:0
	ds_read_b128 v[138:141], v192 offset:0x800
	ds_read_b128 v[142:145], v191 offset:0x800
	ds_read_b128 v[130:133], v192 offset:0x1000
	ds_read_b128 v[134:137], v191 offset:0x1000
	s_mov_b64 s[28:29], 0xc000
	v_lshl_add_u64 v[34:35], v[184:185], 0, s[28:29]
	s_add_i32 m0, s4, 0x6000
	s_mov_b64 s[28:29], 0xe000
	global_load_lds_dwordx4 v[34:35], off
	v_lshl_add_u64 v[34:35], v[184:185], 0, s[28:29]
	s_add_i32 m0, s4, 0xe000
	s_nop 9
	v_cvt_pk_u8_f32 v2, v2, 0, 0
	global_load_lds_dwordx4 v[34:35], off
	v_cvt_pk_u8_f32 v18, v18, 0, 0
	v_cvt_pk_u8_f32 v2, v3, 1, v2
	v_cvt_pk_u8_f32 v18, v19, 1, v18
	v_cvt_pk_u8_f32 v2, v4, 2, v2
	v_cvt_pk_u8_f32 v18, v20, 2, v18
	v_cvt_pk_u8_f32 v158, v5, 3, v2
	v_cvt_pk_u8_f32 v2, v6, 0, 0
	v_cvt_pk_u8_f32 v154, v21, 3, v18
	v_cvt_pk_u8_f32 v18, v22, 0, 0
	v_cvt_pk_u8_f32 v2, v7, 1, v2
	v_cvt_pk_u8_f32 v18, v23, 1, v18
	v_cvt_pk_u8_f32 v2, v8, 2, v2
	v_cvt_pk_u8_f32 v18, v24, 2, v18
	v_cvt_pk_u8_f32 v159, v9, 3, v2
	v_cvt_pk_u8_f32 v2, v10, 0, 0
	v_cvt_pk_u8_f32 v155, v25, 3, v18
	v_cvt_pk_u8_f32 v18, v26, 0, 0
	v_cvt_pk_u8_f32 v2, v11, 1, v2
	v_cvt_pk_u8_f32 v18, v27, 1, v18
	v_cvt_pk_u8_f32 v2, v12, 2, v2
	v_cvt_pk_u8_f32 v18, v28, 2, v18
	v_cvt_pk_u8_f32 v160, v13, 3, v2
	v_cvt_pk_u8_f32 v2, v14, 0, 0
	v_cvt_pk_u8_f32 v156, v29, 3, v18
	v_cvt_pk_u8_f32 v18, v30, 0, 0
	v_cvt_pk_u8_f32 v2, v15, 1, v2
	s_waitcnt vmcnt(2)
	v_cvt_pk_u8_f32 v18, v31, 1, v18
	v_cvt_pk_u8_f32 v2, v16, 2, v2
	v_cvt_pk_u8_f32 v18, v32, 2, v18
	v_cvt_pk_u8_f32 v161, v17, 3, v2
	v_mov_b32_e32 v2, 0
	v_readlane_b32 s46, v255, 41
	s_add_i32 s26, s26, -1
	v_cvt_pk_u8_f32 v157, v33, 3, v18
	s_mov_b32 s27, 0
	v_mov_b32_e32 v3, v2
	v_mov_b32_e32 v4, v2
	v_mov_b32_e32 v5, v2
	v_mov_b32_e32 v6, v2
	v_mov_b32_e32 v7, v2
	v_mov_b32_e32 v8, v2
	v_mov_b32_e32 v9, v2
	v_mov_b32_e32 v10, v2
	v_mov_b32_e32 v11, v2
	v_mov_b32_e32 v12, v2
	v_mov_b32_e32 v13, v2
	v_mov_b32_e32 v14, v2
	v_mov_b32_e32 v15, v2
	v_mov_b32_e32 v16, v2
	v_mov_b32_e32 v17, v2
	v_mov_b32_e32 v18, v2
	v_mov_b32_e32 v19, v2
	v_mov_b32_e32 v20, v2
	v_mov_b32_e32 v21, v2
	v_mov_b32_e32 v22, v2
	v_mov_b32_e32 v23, v2
	v_mov_b32_e32 v24, v2
	v_mov_b32_e32 v25, v2
	v_mov_b32_e32 v26, v2
	v_mov_b32_e32 v27, v2
	v_mov_b32_e32 v28, v2
	v_mov_b32_e32 v29, v2
	v_mov_b32_e32 v30, v2
	v_mov_b32_e32 v31, v2
	v_mov_b32_e32 v32, v2
	v_mov_b32_e32 v33, v2
	v_mov_b32_e32 v34, v2
	v_mov_b32_e32 v35, v2
	v_mov_b32_e32 v36, v2
	v_mov_b32_e32 v37, v2
	v_mov_b32_e32 v38, v2
	v_mov_b32_e32 v39, v2
	v_mov_b32_e32 v40, v2
	v_mov_b32_e32 v41, v2
	v_mov_b32_e32 v42, v2
	v_mov_b32_e32 v43, v2
	v_mov_b32_e32 v44, v2
	v_mov_b32_e32 v45, v2
	v_mov_b32_e32 v46, v2
	v_mov_b32_e32 v47, v2
	v_mov_b32_e32 v48, v2
	v_mov_b32_e32 v49, v2
	v_mov_b32_e32 v178, v2
	v_mov_b32_e32 v179, v2
	v_mov_b32_e32 v180, v2
	v_mov_b32_e32 v181, v2
	v_mov_b32_e32 v50, v2
	v_mov_b32_e32 v51, v2
	v_mov_b32_e32 v52, v2
	v_mov_b32_e32 v53, v2
	v_mov_b32_e32 v54, v2
	v_mov_b32_e32 v55, v2
	v_mov_b32_e32 v56, v2
	v_mov_b32_e32 v57, v2
	v_mov_b32_e32 v58, v2
	v_mov_b32_e32 v59, v2
	v_mov_b32_e32 v60, v2
	v_mov_b32_e32 v61, v2
	v_mov_b32_e32 v62, v2
	v_mov_b32_e32 v63, v2
	v_mov_b32_e32 v64, v2
	v_mov_b32_e32 v65, v2
	v_readlane_b32 s47, v255, 42
	s_add_i32 s29, s5, 0x8000
	s_add_i32 s28, s5, 0xffffa000
.Lrot_diff:
	s_barrier
	s_and_b32 s29, s29, 0xe000
	s_waitcnt lgkmcnt(0)
	v_mfma_scale_f32_32x32x64_f8f6f4 v[82:97], v[162:169], v[122:129], v[66:81], v213, v213 op_sel_hi:[0,0,0]
	v_mfma_scale_f32_32x32x64_f8f6f4 v[98:113], v[170:177], v[122:129], v[66:81], v213, v213 op_sel_hi:[0,0,0]
	v_mfma_scale_f32_32x32x64_f8f6f4 v[50:65], v[154:161], v[146:153], v[50:65], v221, v220 op_sel_hi:[0,0,0] cbsz:1
	v_add_u32_e32 v150, s29, v192
	ds_read_b128 v[146:149], v150 offset:0x1800
	v_add_u32_e32 v162, s29, v191
	ds_read_b128 v[150:153], v162 offset:0x1800
	v_mfma_scale_f32_32x32x64_f8f6f4 v[34:49], v[154:161], v[138:145], v[34:49], v221, v220 op_sel_hi:[0,0,0] cbsz:1
	v_mfma_scale_f32_32x32x64_f8f6f4 v[18:33], v[154:161], v[130:137], v[18:33], v221, v220 op_sel_hi:[0,0,0] cbsz:1
	v_mfma_scale_f32_16x16x128_f8f6f4 v[178:181], v[154:161], v[114:121], v[178:181], v221, v221 op_sel_hi:[0,0,0] cbsz:1
	s_waitcnt lgkmcnt(0)
	v_mfma_scale_f32_32x32x64_f8f6f4 v[2:17], v[154:161], v[146:153], v[2:17], v221, v220 op_sel_hi:[0,0,0] cbsz:1
	s_add_i32 s29, s5, 0xffffc000
	s_and_b32 s29, s29, 0x6000
	s_barrier
	v_add_u32_e32 v130, s29, v190
	ds_read_b128 v[162:165], v130 offset:0
	v_add_u32_e32 v131, s29, v193
	ds_read_b128 v[166:169], v131 offset:0
	ds_read_b128 v[170:173], v130 offset:0x1000
	ds_read_b128 v[174:177], v131 offset:0x1000
	s_and_b32 s28, s28, 0xe000
	v_add_u32_e32 v134, s28, v192
	ds_read_b128 v[146:149], v134 offset:0
	v_add_u32_e32 v154, s28, v191
	ds_read_b128 v[150:153], v154 offset:0
	ds_read_b128 v[138:141], v134 offset:0x800
	ds_read_b128 v[142:145], v154 offset:0x800
	ds_read_b128 v[130:133], v134 offset:0x1000
	ds_read_b128 v[134:137], v154 offset:0x1000
	s_add_i32 s28, s27, 4
	s_min_u32 s80, s28, s26
	s_lshl_b64 s[28:29], s[80:81], 14
	v_lshl_add_u64 v[154:155], v[184:185], 0, s[28:29]
	s_and_b32 s28, s5, 0x6000
	s_add_i32 m0, s4, s28
	s_and_b32 s28, s5, 0xe000
	s_add_i32 s28, s4, s28
	global_load_lds_dwordx4 v[154:155], off
	v_lshl_add_u64 v[154:155], v[154:155], 0, s[48:49]
	s_add_i32 m0, s28, 0x8000
	v_cvt_pk_u8_f32 v82, v82, 0, 0
	global_load_lds_dwordx4 v[154:155], off
	v_cvt_pk_u8_f32 v98, v98, 0, 0
	v_cvt_pk_u8_f32 v82, v83, 1, v82
	v_cvt_pk_u8_f32 v83, v99, 1, v98
	v_cvt_pk_u8_f32 v82, v84, 2, v82
	v_cvt_pk_u8_f32 v83, v100, 2, v83
	v_cvt_pk_u8_f32 v154, v85, 3, v82
	v_cvt_pk_u8_f32 v158, v101, 3, v83
	v_cvt_pk_u8_f32 v82, v86, 0, 0
	v_cvt_pk_u8_f32 v83, v102, 0, 0
	v_cvt_pk_u8_f32 v82, v87, 1, v82
	v_cvt_pk_u8_f32 v83, v103, 1, v83
	v_cvt_pk_u8_f32 v82, v88, 2, v82
	v_cvt_pk_u8_f32 v83, v104, 2, v83
	v_cvt_pk_u8_f32 v155, v89, 3, v82
	v_cvt_pk_u8_f32 v159, v105, 3, v83
	v_cvt_pk_u8_f32 v82, v90, 0, 0
	v_cvt_pk_u8_f32 v83, v106, 0, 0
	v_cvt_pk_u8_f32 v82, v91, 1, v82
	v_cvt_pk_u8_f32 v83, v107, 1, v83
	v_cvt_pk_u8_f32 v82, v92, 2, v82
	v_cvt_pk_u8_f32 v83, v108, 2, v83
	v_cvt_pk_u8_f32 v156, v93, 3, v82
	v_cvt_pk_u8_f32 v160, v109, 3, v83
	v_cvt_pk_u8_f32 v82, v94, 0, 0
	v_cvt_pk_u8_f32 v83, v110, 0, 0
	v_cvt_pk_u8_f32 v82, v95, 1, v82
	v_cvt_pk_u8_f32 v83, v111, 1, v83
	s_waitcnt vmcnt(2)
	v_cvt_pk_u8_f32 v82, v96, 2, v82
	v_cvt_pk_u8_f32 v83, v112, 2, v83
	s_addk_i32 s5, 0x2000
	s_add_i32 s27, s27, 1
	s_add_i32 s29, s5, 0x8000
	s_add_i32 s28, s5, 0xffffa000
	v_cvt_pk_u8_f32 v157, v97, 3, v82
	v_cvt_pk_u8_f32 v161, v113, 3, v83
	s_cmp_eq_u32 s26, s27
	s_cbranch_scc0 .Lrot_diff
	s_barrier
	s_waitcnt vmcnt(0)
	s_lshl_b32 s4, s26, 13
	s_and_b32 s4, s4, 0xe000
	s_waitcnt lgkmcnt(0)
	v_mfma_scale_f32_32x32x64_f8f6f4 v[50:65], v[154:161], v[146:153], v[50:65], v221, v220 op_sel_hi:[0,0,0] cbsz:1
	v_add_u32_e32 v66, s4, v192
	ds_read_b128 v[70:73], v66 offset:0x1800
	v_add_u32_e32 v66, s4, v191
	ds_read_b128 v[74:77], v66 offset:0x1800
	v_mfma_scale_f32_32x32x64_f8f6f4 v[34:49], v[154:161], v[138:145], v[34:49], v221, v220 op_sel_hi:[0,0,0] cbsz:1
	v_mfma_scale_f32_32x32x64_f8f6f4 v[18:33], v[154:161], v[130:137], v[18:33], v221, v220 op_sel_hi:[0,0,0] cbsz:1
	v_mfma_scale_f32_16x16x128_f8f6f4 v[66:69], v[154:161], v[114:121], v[178:181], v221, v221 op_sel_hi:[0,0,0] cbsz:1
	s_waitcnt lgkmcnt(0)
	v_mfma_scale_f32_32x32x64_f8f6f4 v[2:17], v[154:161], v[70:77], v[2:17], v221, v220 op_sel_hi:[0,0,0] cbsz:1
	s_and_b64 vcc, exec, s[38:39]
	s_cbranch_vccz .LBB0_347
	s_barrier
